# v38: v37 + up-GEMM K-loop LDS-DMA staging rebalanced 2/6/2/6 -> 4/4/4/4 pieces per phase (A00 stage moved to phase C, A10 stage to next phase A; vmcnt 8/6/8/6)
# speedup vs baseline: 1.0078x; 1.0078x over previous
.LBB0_1508:
	s_add_u32 s42, s40, 0xfffe0080
	s_addc_u32 s43, s41, -1
	s_add_i32 s68, 0, 0x10000
	s_cmp_eq_u32 s67, 4
	s_cselect_b32 s43, s23, s43
	s_cselect_b32 s42, s29, s42
	v_add_u32_e32 v0, s68, v157
	s_cselect_b32 s45, s31, s66
	s_cselect_b32 s44, s30, s37
	s_add_i32 s70, 0, 0x14000
	ds_read_b128 v[82:85], v0
	ds_read_b128 v[86:89], v0 offset:1024
	ds_read_b128 v[90:93], v0 offset:2048
	ds_read_b128 v[94:97], v0 offset:3072
	v_add_u32_e32 v0, s70, v157
	ds_read_b128 v[160:163], v0
	ds_read_b128 v[164:167], v0 offset:1024
	ds_read_b128 v[168:171], v0 offset:2048
	ds_read_b128 v[172:175], v0 offset:3072
	v_mov_b32_e32 v0, v149
	ds_read_b128 v[176:179], v159
	ds_read_b128 v[180:183], v159 offset:1024
	ds_read_b128 v[184:187], v159 offset:2048
	ds_read_b128 v[188:191], v159 offset:3072
	ds_read_b128 v[192:195], v159 offset:4096
	ds_read_b128 v[196:199], v159 offset:5120
	ds_read_b128 v[200:203], v159 offset:6144
	ds_read_b128 v[204:207], v159 offset:7168
	s_add_i32 m0, s85, 0xc000
	s_nop 0
	global_load_lds_dwordx4 v0, s[40:41]
	v_mov_b32_e32 v0, v153
	s_add_i32 m0, s85, 0xe000
	s_nop 0
	global_load_lds_dwordx4 v0, s[40:41]
	s_waitcnt vmcnt(8)
	s_waitcnt lgkmcnt(0)
	s_barrier
	s_setprio 1
	s_waitcnt lgkmcnt(0)
	v_mfma_i32_16x16x64_i8 v[142:145], v[82:85], v[176:179], v[142:145]
	v_mfma_i32_16x16x64_i8 v[134:137], v[90:93], v[176:179], v[134:137]
	v_mfma_i32_16x16x64_i8 v[126:129], v[82:85], v[184:187], v[126:129]
	v_mfma_i32_16x16x64_i8 v[122:125], v[90:93], v[184:187], v[122:125]
	v_mfma_i32_16x16x64_i8 v[110:113], v[82:85], v[192:195], v[110:113]
	v_mfma_i32_16x16x64_i8 v[106:109], v[90:93], v[192:195], v[106:109]
	v_mfma_i32_16x16x64_i8 v[78:81], v[82:85], v[200:203], v[78:81]
	v_mfma_i32_16x16x64_i8 v[74:77], v[90:93], v[200:203], v[74:77]
	v_mfma_i32_16x16x64_i8 v[142:145], v[86:89], v[180:183], v[142:145]
	v_mfma_i32_16x16x64_i8 v[134:137], v[94:97], v[180:183], v[134:137]
	v_mfma_i32_16x16x64_i8 v[126:129], v[86:89], v[188:191], v[126:129]
	v_mfma_i32_16x16x64_i8 v[122:125], v[94:97], v[188:191], v[122:125]
	v_mfma_i32_16x16x64_i8 v[110:113], v[86:89], v[196:199], v[110:113]
	v_mfma_i32_16x16x64_i8 v[106:109], v[94:97], v[196:199], v[106:109]
	v_mfma_i32_16x16x64_i8 v[78:81], v[86:89], v[204:207], v[78:81]
	v_mfma_i32_16x16x64_i8 v[74:77], v[94:97], v[204:207], v[74:77]
	s_setprio 0
	s_setprio 1
	v_mfma_i32_16x16x64_i8 v[138:141], v[160:163], v[176:179], v[138:141]
	v_mfma_i32_16x16x64_i8 v[130:133], v[168:171], v[176:179], v[130:133]
	v_mfma_i32_16x16x64_i8 v[118:121], v[160:163], v[184:187], v[118:121]
	v_mfma_i32_16x16x64_i8 v[114:117], v[168:171], v[184:187], v[114:117]
	v_mfma_i32_16x16x64_i8 v[102:105], v[160:163], v[192:195], v[102:105]
	v_mfma_i32_16x16x64_i8 v[98:101], v[168:171], v[192:195], v[98:101]
	v_mfma_i32_16x16x64_i8 v[70:73], v[160:163], v[200:203], v[70:73]
	v_mfma_i32_16x16x64_i8 v[66:69], v[168:171], v[200:203], v[66:69]
	v_mfma_i32_16x16x64_i8 v[138:141], v[164:167], v[180:183], v[138:141]
	v_mfma_i32_16x16x64_i8 v[130:133], v[172:175], v[180:183], v[130:133]
	v_mfma_i32_16x16x64_i8 v[118:121], v[164:167], v[188:191], v[118:121]
	v_mfma_i32_16x16x64_i8 v[114:117], v[172:175], v[188:191], v[114:117]
	v_mfma_i32_16x16x64_i8 v[102:105], v[164:167], v[196:199], v[102:105]
	v_mfma_i32_16x16x64_i8 v[98:101], v[172:175], v[196:199], v[98:101]
	v_mfma_i32_16x16x64_i8 v[70:73], v[164:167], v[204:207], v[70:73]
	v_mfma_i32_16x16x64_i8 v[66:69], v[172:175], v[204:207], v[66:69]
	s_setprio 0
	s_barrier
	v_mov_b32_e32 v0, v151
	s_add_i32 s68, s68, s33
	ds_read_b128 v[176:179], v159 offset:16384
	ds_read_b128 v[180:183], v159 offset:17408
	ds_read_b128 v[184:187], v159 offset:18432
	ds_read_b128 v[188:191], v159 offset:19456
	ds_read_b128 v[192:195], v159 offset:20480
	ds_read_b128 v[196:199], v159 offset:21504
	ds_read_b128 v[200:203], v159 offset:22528
	ds_read_b128 v[204:207], v159 offset:23552
	s_mov_b32 m0, s68
	s_nop 0
	global_load_lds_dwordx4 v0, s[44:45]
	v_mov_b32_e32 v0, v155
	s_add_i32 m0, s68, 0x2000
	s_add_u32 s68, s44, 0x20000
	global_load_lds_dwordx4 v0, s[44:45]
	s_addc_u32 s69, s45, 0
	v_mov_b32_e32 v0, v151
	s_add_i32 s70, s70, s33
	s_mov_b32 m0, s70
	s_nop 0
	global_load_lds_dwordx4 v0, s[68:69]
	v_mov_b32_e32 v0, v155
	s_add_i32 m0, s70, 0x2000
	s_nop 0
	global_load_lds_dwordx4 v0, s[68:69]
	s_waitcnt vmcnt(6)
	s_waitcnt lgkmcnt(0)
	s_barrier
	s_setprio 1
	s_waitcnt lgkmcnt(0)
	v_mfma_i32_16x16x64_i8 v[62:65], v[82:85], v[176:179], v[62:65]
	v_mfma_i32_16x16x64_i8 v[58:61], v[90:93], v[176:179], v[58:61]
	v_mfma_i32_16x16x64_i8 v[46:49], v[82:85], v[184:187], v[46:49]
	v_mfma_i32_16x16x64_i8 v[42:45], v[90:93], v[184:187], v[42:45]
	v_mfma_i32_16x16x64_i8 v[30:33], v[82:85], v[192:195], v[30:33]
	v_mfma_i32_16x16x64_i8 v[26:29], v[90:93], v[192:195], v[26:29]
	v_mfma_i32_16x16x64_i8 v[14:17], v[82:85], v[200:203], v[14:17]
	v_mfma_i32_16x16x64_i8 v[10:13], v[90:93], v[200:203], v[10:13]
	v_mfma_i32_16x16x64_i8 v[62:65], v[86:89], v[180:183], v[62:65]
	v_mfma_i32_16x16x64_i8 v[58:61], v[94:97], v[180:183], v[58:61]
	v_mfma_i32_16x16x64_i8 v[46:49], v[86:89], v[188:191], v[46:49]
	v_mfma_i32_16x16x64_i8 v[42:45], v[94:97], v[188:191], v[42:45]
	v_mfma_i32_16x16x64_i8 v[30:33], v[86:89], v[196:199], v[30:33]
	v_mfma_i32_16x16x64_i8 v[26:29], v[94:97], v[196:199], v[26:29]
	v_mfma_i32_16x16x64_i8 v[14:17], v[86:89], v[204:207], v[14:17]
	v_mfma_i32_16x16x64_i8 v[10:13], v[94:97], v[204:207], v[10:13]
	s_setprio 0
	s_setprio 1
	v_mfma_i32_16x16x64_i8 v[54:57], v[160:163], v[176:179], v[54:57]
	v_mfma_i32_16x16x64_i8 v[50:53], v[168:171], v[176:179], v[50:53]
	v_mfma_i32_16x16x64_i8 v[38:41], v[160:163], v[184:187], v[38:41]
	v_mfma_i32_16x16x64_i8 v[34:37], v[168:171], v[184:187], v[34:37]
	v_mfma_i32_16x16x64_i8 v[22:25], v[160:163], v[192:195], v[22:25]
	v_mfma_i32_16x16x64_i8 v[18:21], v[168:171], v[192:195], v[18:21]
	v_mfma_i32_16x16x64_i8 v[6:9], v[160:163], v[200:203], v[6:9]
	v_mfma_i32_16x16x64_i8 v[2:5], v[168:171], v[200:203], v[2:5]
	v_mfma_i32_16x16x64_i8 v[54:57], v[164:167], v[180:183], v[54:57]
	v_mfma_i32_16x16x64_i8 v[50:53], v[172:175], v[180:183], v[50:53]
	v_mfma_i32_16x16x64_i8 v[38:41], v[164:167], v[188:191], v[38:41]
	v_mfma_i32_16x16x64_i8 v[34:37], v[172:175], v[188:191], v[34:37]
	v_mfma_i32_16x16x64_i8 v[22:25], v[164:167], v[196:199], v[22:25]
	v_mfma_i32_16x16x64_i8 v[18:21], v[172:175], v[196:199], v[18:21]
	v_mfma_i32_16x16x64_i8 v[6:9], v[164:167], v[204:207], v[6:9]
	v_mfma_i32_16x16x64_i8 v[2:5], v[172:175], v[204:207], v[2:5]
	s_setprio 0
	s_barrier
	s_add_i32 s70, 0, 0x18000
	v_add_u32_e32 v0, s70, v157
	s_add_i32 s71, 0, 0x1c000
	ds_read_b128 v[82:85], v0
	ds_read_b128 v[86:89], v0 offset:1024
	ds_read_b128 v[90:93], v0 offset:2048
	ds_read_b128 v[94:97], v0 offset:3072
	v_add_u32_e32 v0, s71, v157
	ds_read_b128 v[160:163], v0
	ds_read_b128 v[164:167], v0 offset:1024
	ds_read_b128 v[168:171], v0 offset:2048
	ds_read_b128 v[172:175], v0 offset:3072
	s_add_u32 s68, s42, 0x20000
	ds_read_b128 v[176:179], v159 offset:32768
	ds_read_b128 v[180:183], v159 offset:33792
	ds_read_b128 v[184:187], v159 offset:34816
	ds_read_b128 v[188:191], v159 offset:35840
	ds_read_b128 v[192:195], v159 offset:36864
	ds_read_b128 v[196:199], v159 offset:37888
	ds_read_b128 v[200:203], v159 offset:38912
	ds_read_b128 v[204:207], v159 offset:39936
	s_addc_u32 s69, s43, 0
	v_mov_b32_e32 v0, v149
	s_mov_b32 m0, s85
	s_nop 0
	global_load_lds_dwordx4 v0, s[42:43]
	v_mov_b32_e32 v0, v153
	s_mov_b32 m0, s56
	s_nop 0
	global_load_lds_dwordx4 v0, s[42:43]
	v_mov_b32_e32 v0, v149
	s_mov_b32 m0, s57
	s_nop 0
	global_load_lds_dwordx4 v0, s[68:69]
	v_mov_b32_e32 v0, v153
	s_mov_b32 m0, s58
	s_nop 0
	global_load_lds_dwordx4 v0, s[68:69]
	s_waitcnt vmcnt(8)
	s_waitcnt lgkmcnt(0)
	s_barrier
	s_setprio 1
	s_waitcnt lgkmcnt(0)
	v_mfma_i32_16x16x64_i8 v[142:145], v[82:85], v[176:179], v[142:145]
	v_mfma_i32_16x16x64_i8 v[134:137], v[90:93], v[176:179], v[134:137]
	v_mfma_i32_16x16x64_i8 v[126:129], v[82:85], v[184:187], v[126:129]
	v_mfma_i32_16x16x64_i8 v[122:125], v[90:93], v[184:187], v[122:125]
	v_mfma_i32_16x16x64_i8 v[110:113], v[82:85], v[192:195], v[110:113]
	v_mfma_i32_16x16x64_i8 v[106:109], v[90:93], v[192:195], v[106:109]
	v_mfma_i32_16x16x64_i8 v[78:81], v[82:85], v[200:203], v[78:81]
	v_mfma_i32_16x16x64_i8 v[74:77], v[90:93], v[200:203], v[74:77]
	v_mfma_i32_16x16x64_i8 v[142:145], v[86:89], v[180:183], v[142:145]
	v_mfma_i32_16x16x64_i8 v[134:137], v[94:97], v[180:183], v[134:137]
	v_mfma_i32_16x16x64_i8 v[126:129], v[86:89], v[188:191], v[126:129]
	v_mfma_i32_16x16x64_i8 v[122:125], v[94:97], v[188:191], v[122:125]
	v_mfma_i32_16x16x64_i8 v[110:113], v[86:89], v[196:199], v[110:113]
	v_mfma_i32_16x16x64_i8 v[106:109], v[94:97], v[196:199], v[106:109]
	v_mfma_i32_16x16x64_i8 v[78:81], v[86:89], v[204:207], v[78:81]
	v_mfma_i32_16x16x64_i8 v[74:77], v[94:97], v[204:207], v[74:77]
	s_setprio 0
	s_setprio 1
	v_mfma_i32_16x16x64_i8 v[138:141], v[160:163], v[176:179], v[138:141]
	v_mfma_i32_16x16x64_i8 v[130:133], v[168:171], v[176:179], v[130:133]
	v_mfma_i32_16x16x64_i8 v[118:121], v[160:163], v[184:187], v[118:121]
	v_mfma_i32_16x16x64_i8 v[114:117], v[168:171], v[184:187], v[114:117]
	v_mfma_i32_16x16x64_i8 v[102:105], v[160:163], v[192:195], v[102:105]
	v_mfma_i32_16x16x64_i8 v[98:101], v[168:171], v[192:195], v[98:101]
	v_mfma_i32_16x16x64_i8 v[70:73], v[160:163], v[200:203], v[70:73]
	v_mfma_i32_16x16x64_i8 v[66:69], v[168:171], v[200:203], v[66:69]
	v_mfma_i32_16x16x64_i8 v[138:141], v[164:167], v[180:183], v[138:141]
	v_mfma_i32_16x16x64_i8 v[130:133], v[172:175], v[180:183], v[130:133]
	v_mfma_i32_16x16x64_i8 v[118:121], v[164:167], v[188:191], v[118:121]
	v_mfma_i32_16x16x64_i8 v[114:117], v[172:175], v[188:191], v[114:117]
	v_mfma_i32_16x16x64_i8 v[102:105], v[164:167], v[196:199], v[102:105]
	v_mfma_i32_16x16x64_i8 v[98:101], v[172:175], v[196:199], v[98:101]
	v_mfma_i32_16x16x64_i8 v[70:73], v[164:167], v[204:207], v[70:73]
	v_mfma_i32_16x16x64_i8 v[66:69], v[172:175], v[204:207], v[66:69]
	s_setprio 0
	s_barrier
	v_mov_b32_e32 v0, v151
	ds_read_b128 v[176:179], v159 offset:49152
	ds_read_b128 v[180:183], v159 offset:50176
	ds_read_b128 v[184:187], v159 offset:51200
	ds_read_b128 v[188:191], v159 offset:52224
	ds_read_b128 v[192:195], v159 offset:53248
	ds_read_b128 v[196:199], v159 offset:54272
	ds_read_b128 v[200:203], v159 offset:55296
	ds_read_b128 v[204:207], v159 offset:56320
	s_add_i32 s68, s70, s33
	v_lshl_add_u64 v[146:147], s[44:45], 0, v[0:1]
	v_lshl_add_u64 v[146:147], v[146:147], 0, s[90:91]
	s_mov_b32 m0, s68
	v_mov_b32_e32 v0, v155
	global_load_lds_dwordx4 v[146:147], off
	s_add_i32 m0, s68, 0x2000
	s_nop 0
	v_lshl_add_u64 v[146:147], s[44:45], 0, v[0:1]
	s_add_u32 s44, s44, 0x20080
	v_lshl_add_u64 v[146:147], v[146:147], 0, s[90:91]
	s_addc_u32 s45, s45, 0
	v_mov_b32_e32 v0, v151
	s_add_i32 s68, s71, s33
	global_load_lds_dwordx4 v[146:147], off
	s_mov_b32 m0, s68
	s_nop 0
	global_load_lds_dwordx4 v0, s[44:45]
	v_mov_b32_e32 v0, v155
	s_add_i32 m0, s68, 0x2000
	s_nop 0
	global_load_lds_dwordx4 v0, s[44:45]
	s_waitcnt vmcnt(6)
	s_waitcnt lgkmcnt(0)
	s_barrier
	s_setprio 1
	s_waitcnt lgkmcnt(0)
	v_mfma_i32_16x16x64_i8 v[62:65], v[82:85], v[176:179], v[62:65]
	v_mfma_i32_16x16x64_i8 v[58:61], v[90:93], v[176:179], v[58:61]
	v_mfma_i32_16x16x64_i8 v[46:49], v[82:85], v[184:187], v[46:49]
	v_mfma_i32_16x16x64_i8 v[42:45], v[90:93], v[184:187], v[42:45]
	v_mfma_i32_16x16x64_i8 v[30:33], v[82:85], v[192:195], v[30:33]
	v_mfma_i32_16x16x64_i8 v[26:29], v[90:93], v[192:195], v[26:29]
	v_mfma_i32_16x16x64_i8 v[14:17], v[82:85], v[200:203], v[14:17]
	v_mfma_i32_16x16x64_i8 v[10:13], v[90:93], v[200:203], v[10:13]
	v_mfma_i32_16x16x64_i8 v[62:65], v[86:89], v[180:183], v[62:65]
	v_mfma_i32_16x16x64_i8 v[58:61], v[94:97], v[180:183], v[58:61]
	v_mfma_i32_16x16x64_i8 v[46:49], v[86:89], v[188:191], v[46:49]
	v_mfma_i32_16x16x64_i8 v[42:45], v[94:97], v[188:191], v[42:45]
	v_mfma_i32_16x16x64_i8 v[30:33], v[86:89], v[196:199], v[30:33]
	v_mfma_i32_16x16x64_i8 v[26:29], v[94:97], v[196:199], v[26:29]
	v_mfma_i32_16x16x64_i8 v[14:17], v[86:89], v[204:207], v[14:17]
	v_mfma_i32_16x16x64_i8 v[10:13], v[94:97], v[204:207], v[10:13]
	s_setprio 0
	s_setprio 1
	v_mfma_i32_16x16x64_i8 v[54:57], v[160:163], v[176:179], v[54:57]
	v_mfma_i32_16x16x64_i8 v[50:53], v[168:171], v[176:179], v[50:53]
	v_mfma_i32_16x16x64_i8 v[38:41], v[160:163], v[184:187], v[38:41]
	v_mfma_i32_16x16x64_i8 v[34:37], v[168:171], v[184:187], v[34:37]
	v_mfma_i32_16x16x64_i8 v[22:25], v[160:163], v[192:195], v[22:25]
	v_mfma_i32_16x16x64_i8 v[18:21], v[168:171], v[192:195], v[18:21]
	v_mfma_i32_16x16x64_i8 v[6:9], v[160:163], v[200:203], v[6:9]
	v_mfma_i32_16x16x64_i8 v[2:5], v[168:171], v[200:203], v[2:5]
	v_mfma_i32_16x16x64_i8 v[54:57], v[164:167], v[180:183], v[54:57]
	v_mfma_i32_16x16x64_i8 v[50:53], v[172:175], v[180:183], v[50:53]
	v_mfma_i32_16x16x64_i8 v[38:41], v[164:167], v[188:191], v[38:41]
	v_mfma_i32_16x16x64_i8 v[34:37], v[172:175], v[188:191], v[34:37]
	v_mfma_i32_16x16x64_i8 v[22:25], v[164:167], v[196:199], v[22:25]
	v_mfma_i32_16x16x64_i8 v[18:21], v[172:175], v[196:199], v[18:21]
	v_mfma_i32_16x16x64_i8 v[6:9], v[164:167], v[204:207], v[6:9]
	v_mfma_i32_16x16x64_i8 v[2:5], v[172:175], v[204:207], v[2:5]
	s_setprio 0
	s_barrier
	v_mov_b32_e32 v0, v149
	s_mov_b32 m0, s61
	v_lshl_add_u64 v[146:147], s[42:43], 0, v[0:1]
	v_lshl_add_u64 v[146:147], v[146:147], 0, s[90:91]
	v_mov_b32_e32 v0, v153
	global_load_lds_dwordx4 v[146:147], off
	s_mov_b32 m0, s62
	v_lshl_add_u64 v[146:147], s[42:43], 0, v[0:1]
	v_lshl_add_u64 v[146:147], v[146:147], 0, s[90:91]
	global_load_lds_dwordx4 v[146:147], off
	s_add_i32 s67, s67, 2
	s_add_u32 s40, s40, 0x100
	s_addc_u32 s41, s41, 0
	s_add_u32 s37, s37, 0x100
	s_addc_u32 s66, s66, 0
	s_cmp_gt_u32 s67, 5
	s_cbranch_scc0 .LBB0_1508
	s_lshl_b32 s23, s38, 8
	s_add_i32 s23, s23, s87
	s_mul_i32 s37, s65, 0x5800
	s_mul_hi_i32 s29, s65, 0x5800
	s_add_u32 s37, s59, s37
	s_addc_u32 s29, s60, s29
	s_lshl_b32 s40, s36, 8
	s_ashr_i32 s41, s40, 31
	s_lshl_b64 s[40:41], s[40:41], 2
	s_add_u32 s37, s37, s40
	v_mbcnt_lo_u32_b32 v0, -1, 0
	v_mbcnt_hi_u32_b32 v0, -1, v0
	s_addc_u32 s29, s29, s41
	v_lshrrev_b32_e32 v82, 1, v0
	s_lshl_b32 s38, s72, 2
	v_and_or_b32 v160, v0, 15, s23
	v_and_b32_e32 v162, 24, v82
	s_add_u32 s40, s37, s38
	v_ashrrev_i32_e32 v161, 31, v160
	s_addc_u32 s41, s29, 0
	v_lshlrev_b32_e32 v90, 2, v162
	v_lshl_add_u64 v[146:147], v[160:161], 2, s[20:21]
	global_load_dwordx4 v[86:89], v90, s[40:41] offset:16
	global_load_dwordx4 v[94:97], v90, s[40:41]
	global_load_dwordx4 v[82:85], v90, s[40:41] offset:528
	s_nop 0
	global_load_dwordx4 v[90:93], v90, s[40:41] offset:512
	v_cvt_f32_i32_e32 v173, v143
	global_load_dword v170, v[146:147], off
	global_load_dword v158, v[146:147], off offset:64
	global_load_dword v156, v[146:147], off offset:128
	global_load_dword v154, v[146:147], off offset:192
	global_load_dword v152, v[146:147], off offset:512
	global_load_dword v150, v[146:147], off offset:576
	global_load_dword v148, v[146:147], off offset:640
	global_load_dword v0, v[146:147], off offset:704
	v_cvt_f32_i32_e32 v172, v142
	v_cvt_f32_i32_e32 v143, v145
	v_cvt_f32_i32_e32 v142, v144
	s_lshl_b32 s23, s36, 7
	s_or_b32 s23, s23, s72
	v_or_b32_e32 v146, s23, v162
	v_cvt_f32_i32_e32 v133, v133
	v_cvt_f32_i32_e32 v132, v132
	v_cvt_f32_i32_e32 v131, v131
	v_cvt_f32_i32_e32 v130, v130
	s_mov_b32 s23, 0xc3e00000
	s_movk_i32 s29, 0xb00
	v_cvt_f32_i32_e32 v127, v127
	v_cvt_f32_i32_e32 v126, v126
	v_ashrrev_i32_e32 v147, 31, v146
	v_mov_b64_e32 v[176:177], s[18:19]
	v_mad_i64_i32 v[176:177], s[36:37], v160, s29, v[176:177]
	v_lshl_add_u64 v[176:177], v[176:177], 0, v[146:147]
	s_mov_b32 s41, 0
	s_mov_b32 s40, 0xb000
	v_lshl_add_u64 v[178:179], v[176:177], 0, s[40:41]
	s_mov_b32 s40, 0x16000
	v_lshl_add_u64 v[180:181], v[176:177], 0, s[40:41]
	s_mov_b32 s40, 0x21000
	v_lshl_add_u64 v[182:183], v[176:177], 0, s[40:41]
	s_mov_b32 s40, 0x58000
	v_lshl_add_u64 v[184:185], v[176:177], 0, s[40:41]
	s_mov_b32 s40, 0x63000
	v_lshl_add_u64 v[186:187], v[176:177], 0, s[40:41]
	s_mov_b32 s40, 0x6e000
	v_lshl_add_u64 v[188:189], v[176:177], 0, s[40:41]
	s_mov_b32 s40, 0x79000
	v_lshl_add_u64 v[190:191], v[176:177], 0, s[40:41]
	v_cvt_f32_i32_e32 v129, v129
	v_cvt_f32_i32_e32 v128, v128
	v_cvt_f32_i32_e32 v119, v119
	v_cvt_f32_i32_e32 v118, v118
	v_cvt_f32_i32_e32 v121, v121
	v_cvt_f32_i32_e32 v120, v120
	v_cvt_f32_i32_e32 v123, v123
	v_cvt_f32_i32_e32 v122, v122
	v_cvt_f32_i32_e32 v125, v125
	v_cvt_f32_i32_e32 v124, v124
	v_cvt_f32_i32_e32 v115, v115
	v_cvt_f32_i32_e32 v114, v114
	v_cvt_f32_i32_e32 v117, v117
	v_cvt_f32_i32_e32 v116, v116
	v_cvt_f32_i32_e32 v111, v111
	v_cvt_f32_i32_e32 v110, v110
	v_cvt_f32_i32_e32 v113, v113
	v_cvt_f32_i32_e32 v112, v112
	v_cvt_f32_i32_e32 v103, v103
	v_cvt_f32_i32_e32 v102, v102
	v_cvt_f32_i32_e32 v105, v105
	v_cvt_f32_i32_e32 v104, v104
	v_cvt_f32_i32_e32 v107, v107
	v_cvt_f32_i32_e32 v106, v106
	v_cvt_f32_i32_e32 v109, v109
	v_cvt_f32_i32_e32 v108, v108
	v_cvt_f32_i32_e32 v99, v99
	v_cvt_f32_i32_e32 v98, v98
	v_cvt_f32_i32_e32 v101, v101
	v_cvt_f32_i32_e32 v100, v100
	v_cvt_f32_i32_e32 v79, v79
	v_cvt_f32_i32_e32 v78, v78
	v_readlane_b32 s40, v254, 19
	v_readlane_b32 s41, v254, 20
	s_and_b64 vcc, exec, s[40:41]
	s_cbranch_vccz .LBB0_1511
	s_barrier
